# MLA epilogue: packed bf16 rows staged through the wave's private LDS scratch and written with 8 global_store_dwordx4 instead of 32 global_store_dword
# speedup vs baseline: 1.0038x; 1.0038x over previous
; __device__ __forceinline__ float lane_xor1(float v) { return dpp_f<0xB1>(v); }
; __device__ __forceinline__ int crow(int r, int hi) { return (r & 3) + 8 * (r >> 2) + 4 * hi; }
; __device__ __forceinline__ unsigned cvtpk(float lo, float hi) { unsigned r; asm volatile("v_cvt_pk_bf16_f32 %0, %1, %2" : "=v"(r) : "v"(lo), "v"(hi)); return r; }
; __device__ __forceinline__ void store_o_bf16(const f32x16* o, const float* rli, bf16* Ow, int ldo, int lane, int r32, int hi) {
;   const unsigned loff = (unsigned)((((lane & 1) + 4 * hi) * ldo + (r32 & ~1)) * 2);
; #pragma unroll
;   for (int r = 0; r < 16; r += 2) {
;     char* rowp = (char*)(Ow + (size_t)((r & 3) + 8 * (r >> 2)) * ldo);
; #pragma unroll
;     for (int d0 = 0; d0 < 4; ++d0) {
;       const float a = o[d0][r] * rli[r], b = o[d0][r + 1] * rli[r + 1];
;       const float send = (lane & 1) ? a : b; const float recv = lane_xor1(send);
;       const unsigned w = cvtpk((lane & 1) ? recv : a, (lane & 1) ? b : recv);
;       *(unsigned*)(rowp + loff + d0 * 64) = w; } }
; }
; __device__ __forceinline__ void mla_attn_phase(LAS unsigned char* lds, const bf16* Q, const bf16* KV, const bf16* Z, bf16* Oabc, const float* ropec, const float* ropes, int vcu, int G, int tid) {
;     ...
;             if (hi == 0) li_l[r32] = l_reg;
;             asm volatile("s_waitcnt lgkmcnt(0)" ::: "memory");
;             float rli[16];
; #pragma unroll
;             for (int r = 0; r < 16; ++r) rli[r] = __builtin_amdgcn_rcpf(li_l[crow(r, hi)]);
;             { int lane_ = lane; asm volatile("" : "+v"(lane_)); store_o_bf16(o, rli, Oabc + (tok0 + qb * 256 + wid * 32) * 3072 + 2048 + h * 128, 3072, lane_, lane_ & 31, lane_ >> 5); }
.LBB0_1123:
	s_or_b64 exec, exec, s[6:7]
	s_waitcnt lgkmcnt(0)
	v_add_u32_e32 v0, s26, v206
	ds_read_b128 v[2:5], v0
	ds_read_b128 v[6:9], v0 offset:32
	s_add_u32 s6, s38, s24
	s_addc_u32 s7, s39, s27
	s_mulk_i32 s7, 0x1800
	s_waitcnt lgkmcnt(1)
	v_rcp_f32_e32 v10, v2
	v_rcp_f32_e32 v11, v3
	v_rcp_f32_e32 v12, v4
	v_rcp_f32_e32 v13, v5
	s_waitcnt lgkmcnt(0)
	v_rcp_f32_e32 v14, v6
	ds_read_b128 v[2:5], v0 offset:64
	v_rcp_f32_e32 v15, v7
	v_rcp_f32_e32 v80, v8
	v_rcp_f32_e32 v81, v9
	ds_read_b128 v[6:9], v0 offset:96
	s_mul_hi_u32 s14, s6, 0x1800
	s_add_i32 s14, s14, s7
	s_mulk_i32 s6, 0x1800
	v_mov_b32_e32 v0, v198
	s_add_u32 s6, s8, s6
	s_waitcnt lgkmcnt(1)
	v_rcp_f32_e32 v82, v2
	s_waitcnt lgkmcnt(0)
	v_rcp_f32_e32 v86, v6
	s_addc_u32 s7, s9, s14
	v_and_b32_e32 v6, 1, v0
	v_lshrrev_b32_e32 v2, 3, v0
	s_mov_b32 s14, 0x3ffffc
	v_and_or_b32 v2, v2, s14, v6
	v_mul_u32_u24_e32 v2, 0xc00, v2
	s_add_u32 s6, s6, s35
	v_and_or_b32 v0, v0, 30, v2
	s_addc_u32 s7, s7, 0
	v_lshlrev_b32_e32 v0, 1, v0
	v_rcp_f32_e32 v83, v3
	v_rcp_f32_e32 v87, v7
	v_lshl_add_u64 v[2:3], s[6:7], 0, v[0:1]
	v_lshrrev_b32_e32 v90, 4, v198
	v_mul_u32_u24_e32 v90, 0x1800, v90
	v_and_b32_e32 v91, 15, v198
	v_lshl_add_u32 v90, v91, 4, v90
	v_mov_b32_e32 v91, 0
	v_lshl_add_u64 v[90:91], s[6:7], 0, v[90:91]
	s_mov_b32 s94, 0x29e01000
	v_add_co_u32_e64 v90, s[98:99], s94, v90
	s_nop 1
	v_addc_co_u32_e64 v91, s[98:99], 0, v91, s[98:99]
	v_and_b32_e32 v88, 1, v198
	v_lshrrev_b32_e32 v89, 3, v198
	v_and_b32_e32 v89, 4, v89
	v_add_u32_e32 v88, v88, v89
	v_lshlrev_b32_e32 v88, 8, v88
	v_and_b32_e32 v89, 30, v198
	v_lshl_add_u32 v88, v89, 1, v88
	v_add_u32_e32 v88, s25, v88
	v_mul_f32_e32 v0, v64, v10
	v_mul_f32_e32 v7, v65, v11
	v_cmp_eq_u32_e32 vcc, 0, v6
	s_mov_b64 s[6:7], 0x29e01000
	v_rcp_f32_e32 v84, v4
	v_cndmask_b32_e32 v6, v0, v7, vcc
	v_rcp_f32_e32 v85, v5
	v_lshl_add_u64 v[4:5], v[2:3], 0, s[6:7]
	v_mov_b32_dpp v6, v6 quad_perm:[1,0,3,2] row_mask:0xf bank_mask:0xf bound_ctrl:1
	v_cndmask_b32_e32 v0, v6, v0, vcc
	v_cndmask_b32_e32 v6, v7, v6, vcc
	s_mov_b32 s6, 0x29e01000
	v_cvt_pk_bf16_f32 v0, v0, v6
	v_add_co_u32_e64 v6, s[6:7], s6, v2
	v_rcp_f32_e32 v8, v8
	s_nop 0
	v_addc_co_u32_e64 v7, s[6:7], 0, v3, s[6:7]
	ds_write_b32 v88, v0 offset:0
	v_mul_f32_e32 v0, v48, v10
	v_mul_f32_e32 v6, v49, v11
	v_cndmask_b32_e32 v7, v0, v6, vcc
	s_mov_b32 s6, 0x29e04000
	v_rcp_f32_e32 v9, v9
	v_mov_b32_dpp v7, v7 quad_perm:[1,0,3,2] row_mask:0xf bank_mask:0xf bound_ctrl:1
	v_cndmask_b32_e32 v0, v7, v0, vcc
	v_cndmask_b32_e32 v6, v6, v7, vcc
	v_cvt_pk_bf16_f32 v0, v0, v6
	ds_write_b32 v88, v0 offset:64
	v_mul_f32_e32 v0, v32, v10
	v_mul_f32_e32 v6, v33, v11
	v_cndmask_b32_e32 v7, v0, v6, vcc
	s_nop 1
	v_mov_b32_dpp v7, v7 quad_perm:[1,0,3,2] row_mask:0xf bank_mask:0xf bound_ctrl:1
	v_cndmask_b32_e32 v0, v7, v0, vcc
	v_cndmask_b32_e32 v6, v6, v7, vcc
	v_cvt_pk_bf16_f32 v0, v0, v6
	ds_write_b32 v88, v0 offset:128
	v_mul_f32_e32 v0, v16, v10
	v_mul_f32_e32 v6, v17, v11
	v_cndmask_b32_e32 v7, v0, v6, vcc
	s_nop 1
	v_mov_b32_dpp v7, v7 quad_perm:[1,0,3,2] row_mask:0xf bank_mask:0xf bound_ctrl:1
	v_cndmask_b32_e32 v0, v7, v0, vcc
	v_cndmask_b32_e32 v6, v6, v7, vcc
	v_cvt_pk_bf16_f32 v0, v0, v6
	ds_write_b32 v88, v0 offset:192
	v_mul_f32_e32 v0, v66, v12
	v_mul_f32_e32 v4, v67, v13
	v_cndmask_b32_e32 v5, v0, v4, vcc
	v_mul_f32_e32 v6, v51, v13
	s_nop 0
	v_mov_b32_dpp v5, v5 quad_perm:[1,0,3,2] row_mask:0xf bank_mask:0xf bound_ctrl:1
	v_cndmask_b32_e32 v0, v5, v0, vcc
	v_cndmask_b32_e32 v4, v4, v5, vcc
	v_cvt_pk_bf16_f32 v0, v0, v4
	v_add_co_u32_e64 v4, s[6:7], s6, v2
	s_nop 1
	v_addc_co_u32_e64 v5, s[6:7], 0, v3, s[6:7]
	ds_write_b32 v88, v0 offset:512
	v_mul_f32_e32 v0, v50, v12
	v_cndmask_b32_e32 v7, v0, v6, vcc
	s_mov_b32 s6, 0x29e0d000
	s_nop 0
	v_mov_b32_dpp v7, v7 quad_perm:[1,0,3,2] row_mask:0xf bank_mask:0xf bound_ctrl:1
	v_cndmask_b32_e32 v0, v7, v0, vcc
	v_cndmask_b32_e32 v6, v6, v7, vcc
	v_cvt_pk_bf16_f32 v0, v0, v6
	ds_write_b32 v88, v0 offset:576
	v_mul_f32_e32 v0, v34, v12
	v_mul_f32_e32 v6, v35, v13
	v_cndmask_b32_e32 v7, v0, v6, vcc
	s_nop 1
	v_mov_b32_dpp v7, v7 quad_perm:[1,0,3,2] row_mask:0xf bank_mask:0xf bound_ctrl:1
	v_cndmask_b32_e32 v0, v7, v0, vcc
	v_cndmask_b32_e32 v6, v6, v7, vcc
	v_cvt_pk_bf16_f32 v0, v0, v6
	ds_write_b32 v88, v0 offset:640
	v_mul_f32_e32 v0, v18, v12
	v_mul_f32_e32 v6, v19, v13
	v_cndmask_b32_e32 v7, v0, v6, vcc
	s_nop 1
	v_mov_b32_dpp v7, v7 quad_perm:[1,0,3,2] row_mask:0xf bank_mask:0xf bound_ctrl:1
	v_cndmask_b32_e32 v0, v7, v0, vcc
	v_cndmask_b32_e32 v6, v6, v7, vcc
	v_cvt_pk_bf16_f32 v0, v0, v6
	ds_write_b32 v88, v0 offset:704
	v_mul_f32_e32 v0, v68, v14
	v_mul_f32_e32 v4, v69, v15
	v_cndmask_b32_e32 v5, v0, v4, vcc
	v_mul_f32_e32 v6, v53, v15
	s_nop 0
	v_mov_b32_dpp v5, v5 quad_perm:[1,0,3,2] row_mask:0xf bank_mask:0xf bound_ctrl:1
	v_cndmask_b32_e32 v0, v5, v0, vcc
	v_cndmask_b32_e32 v4, v4, v5, vcc
	v_cvt_pk_bf16_f32 v0, v0, v4
	v_add_co_u32_e64 v4, s[6:7], s6, v2
	s_nop 1
	v_addc_co_u32_e64 v5, s[6:7], 0, v3, s[6:7]
	ds_write_b32 v88, v0 offset:2048
	v_mul_f32_e32 v0, v52, v14
	v_cndmask_b32_e32 v7, v0, v6, vcc
	s_mov_b32 s6, 0x29e10000
	s_nop 0
	v_mov_b32_dpp v7, v7 quad_perm:[1,0,3,2] row_mask:0xf bank_mask:0xf bound_ctrl:1
	v_cndmask_b32_e32 v0, v7, v0, vcc
	v_cndmask_b32_e32 v6, v6, v7, vcc
	v_cvt_pk_bf16_f32 v0, v0, v6
	ds_write_b32 v88, v0 offset:2112
	v_mul_f32_e32 v0, v36, v14
	v_mul_f32_e32 v6, v37, v15
	v_cndmask_b32_e32 v7, v0, v6, vcc
	s_nop 1
	v_mov_b32_dpp v7, v7 quad_perm:[1,0,3,2] row_mask:0xf bank_mask:0xf bound_ctrl:1
	v_cndmask_b32_e32 v0, v7, v0, vcc
	v_cndmask_b32_e32 v6, v6, v7, vcc
	v_cvt_pk_bf16_f32 v0, v0, v6
; __device__ __forceinline__ float lane_xor1(float v) { return dpp_f<0xB1>(v); }
; __device__ __forceinline__ unsigned cvtpk(float lo, float hi) { unsigned r; asm volatile("v_cvt_pk_bf16_f32 %0, %1, %2" : "=v"(r) : "v"(lo), "v"(hi)); return r; }
; __device__ __forceinline__ void store_o_bf16(const f32x16* o, const float* rli, bf16* Ow, int ldo, int lane, int r32, int hi) {
;     ...
;   for (int r = 0; r < 16; r += 2) {
;     char* rowp = (char*)(Ow + (size_t)((r & 3) + 8 * (r >> 2)) * ldo);
; #pragma unroll
;     for (int d0 = 0; d0 < 4; ++d0) {
;       const float a = o[d0][r] * rli[r], b = o[d0][r + 1] * rli[r + 1];
;       const float send = (lane & 1) ? a : b; const float recv = lane_xor1(send);
;       const unsigned w = cvtpk((lane & 1) ? recv : a, (lane & 1) ? b : recv);
;       *(unsigned*)(rowp + loff + d0 * 64) = w; } }
	ds_write_b32 v88, v0 offset:2176
	v_mul_f32_e32 v0, v20, v14
	v_mul_f32_e32 v6, v21, v15
	v_cndmask_b32_e32 v7, v0, v6, vcc
	s_nop 1
	v_mov_b32_dpp v7, v7 quad_perm:[1,0,3,2] row_mask:0xf bank_mask:0xf bound_ctrl:1
	v_cndmask_b32_e32 v0, v7, v0, vcc
	v_cndmask_b32_e32 v6, v6, v7, vcc
	v_cvt_pk_bf16_f32 v0, v0, v6
	ds_write_b32 v88, v0 offset:2240
	v_mul_f32_e32 v0, v70, v80
	v_mul_f32_e32 v4, v71, v81
	v_cndmask_b32_e32 v5, v0, v4, vcc
	v_mul_f32_e32 v6, v55, v81
	s_nop 0
	v_mov_b32_dpp v5, v5 quad_perm:[1,0,3,2] row_mask:0xf bank_mask:0xf bound_ctrl:1
	v_cndmask_b32_e32 v0, v5, v0, vcc
	v_cndmask_b32_e32 v4, v4, v5, vcc
	v_cvt_pk_bf16_f32 v0, v0, v4
	v_add_co_u32_e64 v4, s[6:7], s6, v2
	s_nop 1
	v_addc_co_u32_e64 v5, s[6:7], 0, v3, s[6:7]
	ds_write_b32 v88, v0 offset:2560
	v_mul_f32_e32 v0, v54, v80
	v_cndmask_b32_e32 v7, v0, v6, vcc
	s_mov_b32 s6, 0x29e19000
	s_nop 0
	v_mov_b32_dpp v7, v7 quad_perm:[1,0,3,2] row_mask:0xf bank_mask:0xf bound_ctrl:1
	v_cndmask_b32_e32 v0, v7, v0, vcc
	v_cndmask_b32_e32 v6, v6, v7, vcc
	v_cvt_pk_bf16_f32 v0, v0, v6
	ds_write_b32 v88, v0 offset:2624
	v_mul_f32_e32 v0, v38, v80
	v_mul_f32_e32 v6, v39, v81
	v_cndmask_b32_e32 v7, v0, v6, vcc
	s_nop 1
	v_mov_b32_dpp v7, v7 quad_perm:[1,0,3,2] row_mask:0xf bank_mask:0xf bound_ctrl:1
	v_cndmask_b32_e32 v0, v7, v0, vcc
	v_cndmask_b32_e32 v6, v6, v7, vcc
	v_cvt_pk_bf16_f32 v0, v0, v6
	ds_write_b32 v88, v0 offset:2688
	v_mul_f32_e32 v0, v22, v80
	v_mul_f32_e32 v6, v23, v81
	v_cndmask_b32_e32 v7, v0, v6, vcc
	s_nop 1
	v_mov_b32_dpp v7, v7 quad_perm:[1,0,3,2] row_mask:0xf bank_mask:0xf bound_ctrl:1
	v_cndmask_b32_e32 v0, v7, v0, vcc
	v_cndmask_b32_e32 v6, v6, v7, vcc
	v_cvt_pk_bf16_f32 v0, v0, v6
	ds_write_b32 v88, v0 offset:2752
	ds_read_b128 v[92:95], v214
	ds_read_b128 v[96:99], v214 offset:1024
	ds_read_b128 v[100:103], v214 offset:2048
	ds_read_b128 v[104:107], v214 offset:3072
	s_waitcnt lgkmcnt(3)
	global_store_dwordx4 v[90:91], v[92:95], off
	s_mov_b32 s94, 0x6000
	v_add_co_u32_e64 v108, s[98:99], s94, v90
	s_nop 1
	v_addc_co_u32_e64 v109, s[98:99], 0, v91, s[98:99]
	s_waitcnt lgkmcnt(2)
	global_store_dwordx4 v[108:109], v[96:99], off
	s_mov_b32 s94, 0xc000
	v_add_co_u32_e64 v110, s[98:99], s94, v90
	s_nop 1
	v_addc_co_u32_e64 v111, s[98:99], 0, v91, s[98:99]
	s_waitcnt lgkmcnt(1)
	global_store_dwordx4 v[110:111], v[100:103], off
	s_mov_b32 s94, 0x12000
	v_add_co_u32_e64 v108, s[98:99], s94, v90
	s_nop 1
	v_addc_co_u32_e64 v109, s[98:99], 0, v91, s[98:99]
	s_waitcnt lgkmcnt(0)
; __device__ __forceinline__ float lane_xor1(float v) { return dpp_f<0xB1>(v); }
; __device__ __forceinline__ unsigned cvtpk(float lo, float hi) { unsigned r; asm volatile("v_cvt_pk_bf16_f32 %0, %1, %2" : "=v"(r) : "v"(lo), "v"(hi)); return r; }
; __device__ __forceinline__ void store_o_bf16(const f32x16* o, const float* rli, bf16* Ow, int ldo, int lane, int r32, int hi) {
;     ...
;   for (int r = 0; r < 16; r += 2) {
;     char* rowp = (char*)(Ow + (size_t)((r & 3) + 8 * (r >> 2)) * ldo);
; #pragma unroll
;     for (int d0 = 0; d0 < 4; ++d0) {
;       const float a = o[d0][r] * rli[r], b = o[d0][r + 1] * rli[r + 1];
;       const float send = (lane & 1) ? a : b; const float recv = lane_xor1(send);
;       const unsigned w = cvtpk((lane & 1) ? recv : a, (lane & 1) ? b : recv);
;       *(unsigned*)(rowp + loff + d0 * 64) = w; } }
	global_store_dwordx4 v[108:109], v[104:107], off
	v_mul_f32_e32 v0, v72, v82
	v_mul_f32_e32 v4, v73, v83
	v_cndmask_b32_e32 v5, v0, v4, vcc
	v_mul_f32_e32 v6, v57, v83
	s_nop 0
	v_mov_b32_dpp v5, v5 quad_perm:[1,0,3,2] row_mask:0xf bank_mask:0xf bound_ctrl:1
	v_cndmask_b32_e32 v0, v5, v0, vcc
	v_cndmask_b32_e32 v4, v4, v5, vcc
	v_cvt_pk_bf16_f32 v0, v0, v4
	v_add_co_u32_e64 v4, s[6:7], s6, v2
	s_nop 1
	v_addc_co_u32_e64 v5, s[6:7], 0, v3, s[6:7]
	ds_write_b32 v88, v0 offset:0
	v_mul_f32_e32 v0, v56, v82
	v_cndmask_b32_e32 v7, v0, v6, vcc
	s_mov_b32 s6, 0x29e1c000
	s_nop 0
	v_mov_b32_dpp v7, v7 quad_perm:[1,0,3,2] row_mask:0xf bank_mask:0xf bound_ctrl:1
	v_cndmask_b32_e32 v0, v7, v0, vcc
	v_cndmask_b32_e32 v6, v6, v7, vcc
	v_cvt_pk_bf16_f32 v0, v0, v6
	ds_write_b32 v88, v0 offset:64
	v_mul_f32_e32 v0, v40, v82
	v_mul_f32_e32 v6, v41, v83
	v_cndmask_b32_e32 v7, v0, v6, vcc
	s_nop 1
	v_mov_b32_dpp v7, v7 quad_perm:[1,0,3,2] row_mask:0xf bank_mask:0xf bound_ctrl:1
	v_cndmask_b32_e32 v0, v7, v0, vcc
	v_cndmask_b32_e32 v6, v6, v7, vcc
	v_cvt_pk_bf16_f32 v0, v0, v6
	ds_write_b32 v88, v0 offset:128
	v_mul_f32_e32 v0, v24, v82
	v_mul_f32_e32 v6, v25, v83
	v_cndmask_b32_e32 v7, v0, v6, vcc
	s_nop 1
	v_mov_b32_dpp v7, v7 quad_perm:[1,0,3,2] row_mask:0xf bank_mask:0xf bound_ctrl:1
	v_cndmask_b32_e32 v0, v7, v0, vcc
	v_cndmask_b32_e32 v6, v6, v7, vcc
	v_cvt_pk_bf16_f32 v0, v0, v6
	ds_write_b32 v88, v0 offset:192
	v_mul_f32_e32 v0, v74, v84
	v_mul_f32_e32 v4, v75, v85
	v_cndmask_b32_e32 v5, v0, v4, vcc
	v_mul_f32_e32 v6, v59, v85
	s_nop 0
	v_mov_b32_dpp v5, v5 quad_perm:[1,0,3,2] row_mask:0xf bank_mask:0xf bound_ctrl:1
	v_cndmask_b32_e32 v0, v5, v0, vcc
	v_cndmask_b32_e32 v4, v4, v5, vcc
	v_cvt_pk_bf16_f32 v0, v0, v4
	v_add_co_u32_e64 v4, s[6:7], s6, v2
	s_nop 1
	v_addc_co_u32_e64 v5, s[6:7], 0, v3, s[6:7]
	ds_write_b32 v88, v0 offset:512
	v_mul_f32_e32 v0, v58, v84
	v_cndmask_b32_e32 v7, v0, v6, vcc
	s_mov_b32 s6, 0x29e25000
	s_nop 0
	v_mov_b32_dpp v7, v7 quad_perm:[1,0,3,2] row_mask:0xf bank_mask:0xf bound_ctrl:1
	v_cndmask_b32_e32 v0, v7, v0, vcc
	v_cndmask_b32_e32 v6, v6, v7, vcc
	v_cvt_pk_bf16_f32 v0, v0, v6
	ds_write_b32 v88, v0 offset:576
	v_mul_f32_e32 v0, v42, v84
	v_mul_f32_e32 v6, v43, v85
	v_cndmask_b32_e32 v7, v0, v6, vcc
	s_nop 1
	v_mov_b32_dpp v7, v7 quad_perm:[1,0,3,2] row_mask:0xf bank_mask:0xf bound_ctrl:1
	v_cndmask_b32_e32 v0, v7, v0, vcc
	v_cndmask_b32_e32 v6, v6, v7, vcc
	v_cvt_pk_bf16_f32 v0, v0, v6
	ds_write_b32 v88, v0 offset:640
	v_mul_f32_e32 v0, v26, v84
	v_mul_f32_e32 v6, v27, v85
	v_cndmask_b32_e32 v7, v0, v6, vcc
	s_nop 1
	v_mov_b32_dpp v7, v7 quad_perm:[1,0,3,2] row_mask:0xf bank_mask:0xf bound_ctrl:1
	v_cndmask_b32_e32 v0, v7, v0, vcc
	v_cndmask_b32_e32 v6, v6, v7, vcc
	v_cvt_pk_bf16_f32 v0, v0, v6
	ds_write_b32 v88, v0 offset:704
	v_mul_f32_e32 v0, v76, v86
	v_mul_f32_e32 v4, v77, v87
	v_cndmask_b32_e32 v5, v0, v4, vcc
	v_mul_f32_e32 v6, v61, v87
	s_nop 0
	v_mov_b32_dpp v5, v5 quad_perm:[1,0,3,2] row_mask:0xf bank_mask:0xf bound_ctrl:1
	v_cndmask_b32_e32 v0, v5, v0, vcc
	v_cndmask_b32_e32 v4, v4, v5, vcc
	v_cvt_pk_bf16_f32 v0, v0, v4
	v_add_co_u32_e64 v4, s[6:7], s6, v2
	s_nop 1
	v_addc_co_u32_e64 v5, s[6:7], 0, v3, s[6:7]
	ds_write_b32 v88, v0 offset:2048
	v_mul_f32_e32 v0, v60, v86
	v_cndmask_b32_e32 v7, v0, v6, vcc
	s_mov_b32 s6, 0x29e28000
	v_add_co_u32_e64 v2, s[6:7], s6, v2
	v_mov_b32_dpp v7, v7 quad_perm:[1,0,3,2] row_mask:0xf bank_mask:0xf bound_ctrl:1
	v_cndmask_b32_e32 v0, v7, v0, vcc
	v_cndmask_b32_e32 v6, v6, v7, vcc
	v_cvt_pk_bf16_f32 v0, v0, v6
	ds_write_b32 v88, v0 offset:2112
	v_mul_f32_e32 v0, v44, v86
	v_mul_f32_e32 v6, v45, v87
	v_cndmask_b32_e32 v7, v0, v6, vcc
	v_addc_co_u32_e64 v3, s[6:7], 0, v3, s[6:7]
	s_nop 0
	v_mov_b32_dpp v7, v7 quad_perm:[1,0,3,2] row_mask:0xf bank_mask:0xf bound_ctrl:1
	v_cndmask_b32_e32 v0, v7, v0, vcc
	v_cndmask_b32_e32 v6, v6, v7, vcc
	v_cvt_pk_bf16_f32 v0, v0, v6
	ds_write_b32 v88, v0 offset:2176
	v_mul_f32_e32 v0, v28, v86
	v_mul_f32_e32 v6, v29, v87
	v_cndmask_b32_e32 v7, v0, v6, vcc
	s_mov_b64 s[6:7], 0
	s_nop 0
	v_mov_b32_dpp v7, v7 quad_perm:[1,0,3,2] row_mask:0xf bank_mask:0xf bound_ctrl:1
	v_cndmask_b32_e32 v0, v7, v0, vcc
	v_cndmask_b32_e32 v6, v6, v7, vcc
	v_cvt_pk_bf16_f32 v0, v0, v6
	ds_write_b32 v88, v0 offset:2240
	v_mul_f32_e32 v0, v78, v8
	v_mul_f32_e32 v4, v79, v9
	v_cndmask_b32_e32 v5, v0, v4, vcc
	s_nop 1
	v_mov_b32_dpp v5, v5 quad_perm:[1,0,3,2] row_mask:0xf bank_mask:0xf bound_ctrl:1
	v_cndmask_b32_e32 v0, v5, v0, vcc
	v_cndmask_b32_e32 v4, v4, v5, vcc
	v_cvt_pk_bf16_f32 v0, v0, v4
	ds_write_b32 v88, v0 offset:2560
	v_mul_f32_e32 v0, v62, v8
	v_mul_f32_e32 v4, v63, v9
	v_cndmask_b32_e32 v5, v0, v4, vcc
	s_nop 1
	v_mov_b32_dpp v5, v5 quad_perm:[1,0,3,2] row_mask:0xf bank_mask:0xf bound_ctrl:1
	v_cndmask_b32_e32 v0, v5, v0, vcc
	v_cndmask_b32_e32 v4, v4, v5, vcc
	v_cvt_pk_bf16_f32 v0, v0, v4
	ds_write_b32 v88, v0 offset:2624
	v_mul_f32_e32 v0, v46, v8
	v_mul_f32_e32 v4, v47, v9
	v_cndmask_b32_e32 v5, v0, v4, vcc
	s_nop 1
	v_mov_b32_dpp v5, v5 quad_perm:[1,0,3,2] row_mask:0xf bank_mask:0xf bound_ctrl:1
	v_cndmask_b32_e32 v0, v5, v0, vcc
	v_cndmask_b32_e32 v4, v4, v5, vcc
	v_cvt_pk_bf16_f32 v0, v0, v4
	ds_write_b32 v88, v0 offset:2688
	v_mul_f32_e32 v0, v30, v8
	v_mul_f32_e32 v4, v31, v9
	v_cndmask_b32_e32 v5, v0, v4, vcc
	s_nop 1
	v_mov_b32_dpp v5, v5 quad_perm:[1,0,3,2] row_mask:0xf bank_mask:0xf bound_ctrl:1
	v_cndmask_b32_e32 v0, v5, v0, vcc
	v_cndmask_b32_e32 v4, v4, v5, vcc
	s_and_b64 vcc, exec, s[12:13]
	v_cvt_pk_bf16_f32 v0, v0, v4
	ds_write_b32 v88, v0 offset:2752
	ds_read_b128 v[236:239], v214
	ds_read_b128 v[240:243], v214 offset:1024
	ds_read_b128 v[244:247], v214 offset:2048
	ds_read_b128 v[248:251], v214 offset:3072
	s_mov_b32 s94, 0x18000
	v_add_co_u32_e64 v110, s[98:99], s94, v90
	s_nop 1
	v_addc_co_u32_e64 v111, s[98:99], 0, v91, s[98:99]
	s_waitcnt lgkmcnt(3)
	global_store_dwordx4 v[110:111], v[236:239], off
	s_mov_b32 s94, 0x1e000
	v_add_co_u32_e64 v108, s[98:99], s94, v90
	s_nop 1
	v_addc_co_u32_e64 v109, s[98:99], 0, v91, s[98:99]
	s_waitcnt lgkmcnt(2)
	global_store_dwordx4 v[108:109], v[240:243], off
	s_mov_b32 s94, 0x24000
	v_add_co_u32_e64 v110, s[98:99], s94, v90
	s_nop 1
	v_addc_co_u32_e64 v111, s[98:99], 0, v91, s[98:99]
	s_waitcnt lgkmcnt(1)
	global_store_dwordx4 v[110:111], v[244:247], off
	s_mov_b32 s94, 0x2a000
	v_add_co_u32_e64 v108, s[98:99], s94, v90
	s_nop 1
	v_addc_co_u32_e64 v109, s[98:99], 0, v91, s[98:99]
	s_waitcnt lgkmcnt(0)
	global_store_dwordx4 v[108:109], v[248:251], off
	s_cbranch_vccnz .LBB0_1121
